# MoE2: nontemporal hint on the expert-output stores of the first 136 row panels only (written early, evicted before the combine phase reads them)
# baseline (speedup 1.0000x reference)
.LBB0_2154:
	v_lshl_or_b32 v18, s1, 8, v183
	s_ashr_i32 s1, s0, 31
	s_lshl_b64 s[0:1], s[0:1], 13
	s_add_u32 s0, s44, s0
	s_addc_u32 s1, s45, s1
	s_cmp_lt_u32 s77, 136
	s_cselect_b32 s96, 1, 0
	v_ashrrev_i32_e32 v19, 31, v18
	v_cndmask_b32_e64 v3, 0, 1, s[20:21]
	v_lshl_add_u64 v[20:21], v[18:19], 2, s[0:1]
	v_mov_b32_e32 v2, 0
	v_cmp_ne_u32_e64 s[0:1], 1, v3
	s_andn2_b64 vcc, exec, s[20:21]
	v_mov_b32_e32 v6, 0
	v_mov_b32_e32 v7, 0
	v_mov_b32_e32 v8, 0
	v_mov_b32_e32 v9, 0
	s_nop 15
	s_nop 15
	s_nop 15
	s_nop 15
	s_cbranch_vccnz .LBB0_2156
	v_mov_b32_e32 v6, v238
	v_mov_b32_e32 v7, v239
	v_mov_b32_e32 v8, v240
	v_mov_b32_e32 v9, v241

.LBB0_2162:
	v_lshl_add_u32 v24, s77, 8, v1
	v_ashrrev_i32_e32 v25, 31, v24
	v_lshlrev_b64 v[20:21], 12, v[24:25]
	v_lshl_add_u64 v[20:21], s[10:11], 0, v[20:21]
	v_lshlrev_b64 v[26:27], 1, v[18:19]
	v_lshl_add_u64 v[18:19], v[20:21], 0, v[26:27]
	v_pk_fma_f32 v[20:21], v[158:159], s[26:27], v[6:7] op_sel_hi:[1,0,1]
	v_pk_fma_f32 v[22:23], v[160:161], s[26:27], v[8:9] op_sel_hi:[1,0,1]
	v_cvt_pk_bf16_f32 v20, v20, v21
	v_pk_fma_f32 v[28:29], v[156:157], s[26:27], v[4:5] op_sel_hi:[1,0,1]
	v_cvt_pk_bf16_f32 v21, v22, v23
	v_pk_fma_f32 v[30:31], v[154:155], s[26:27], v[2:3] op_sel_hi:[1,0,1]
	v_pk_fma_f32 v[32:33], v[138:139], s[26:27], v[2:3] op_sel_hi:[1,0,1]
	v_cvt_pk_bf16_f32 v22, v30, v31
	v_cvt_pk_bf16_f32 v23, v28, v29
	s_bitcmp1_b32 s96, 0
	s_cbranch_scc1 .Lyb_nt_0
	global_store_dwordx4 v[18:19], v[20:23], off
	s_branch .Lyb_d_0
.Lyb_nt_0:
	global_store_dwordx4 v[18:19], v[20:23], off nt
.Lyb_d_0:
	v_pk_fma_f32 v[28:29], v[144:145], s[26:27], v[12:13] op_sel_hi:[1,0,1]
	v_pk_fma_f32 v[30:31], v[142:143], s[26:27], v[10:11] op_sel_hi:[1,0,1]
	v_pk_fma_f32 v[20:21], v[150:151], s[26:27], v[14:15] op_sel_hi:[1,0,1]
	v_pk_fma_f32 v[22:23], v[152:153], s[26:27], v[16:17] op_sel_hi:[1,0,1]
	v_cvt_pk_bf16_f32 v20, v20, v21
	s_mov_b64 s[0:1], -1
	v_cvt_pk_bf16_f32 v21, v22, v23
	v_cvt_pk_bf16_f32 v22, v30, v31
	v_cvt_pk_bf16_f32 v23, v28, v29
	s_bitcmp1_b32 s96, 0
	s_cbranch_scc1 .Lyb_nt_1
	global_store_dwordx4 v[18:19], v[20:23], off offset:256
	s_branch .Lyb_d_1
.Lyb_nt_1:
	global_store_dwordx4 v[18:19], v[20:23], off offset:256 nt
.Lyb_d_1:
	v_pk_fma_f32 v[30:31], v[140:141], s[26:27], v[4:5] op_sel_hi:[1,0,1]
	s_nop 0
	v_or_b32_e32 v20, 16, v24
	v_ashrrev_i32_e32 v21, 31, v20
	v_lshlrev_b64 v[20:21], 12, v[20:21]
	v_lshl_add_u64 v[20:21], s[10:11], 0, v[20:21]
	v_lshl_add_u64 v[28:29], v[20:21], 0, v[26:27]
	v_pk_fma_f32 v[20:21], v[146:147], s[26:27], v[6:7] op_sel_hi:[1,0,1]
	v_pk_fma_f32 v[22:23], v[148:149], s[26:27], v[8:9] op_sel_hi:[1,0,1]
	v_cvt_pk_bf16_f32 v20, v20, v21
	s_nop 0
	v_cvt_pk_bf16_f32 v21, v22, v23
	v_cvt_pk_bf16_f32 v22, v32, v33
	v_cvt_pk_bf16_f32 v23, v30, v31
	s_bitcmp1_b32 s96, 0
	s_cbranch_scc1 .Lyb_nt_2
	global_store_dwordx4 v[28:29], v[20:23], off
	s_branch .Lyb_d_2
.Lyb_nt_2:
	global_store_dwordx4 v[28:29], v[20:23], off nt
.Lyb_d_2:
	v_pk_fma_f32 v[30:31], v[128:129], s[26:27], v[12:13] op_sel_hi:[1,0,1]
	v_pk_fma_f32 v[32:33], v[126:127], s[26:27], v[10:11] op_sel_hi:[1,0,1]
	v_pk_fma_f32 v[20:21], v[134:135], s[26:27], v[14:15] op_sel_hi:[1,0,1]
	v_pk_fma_f32 v[22:23], v[136:137], s[26:27], v[16:17] op_sel_hi:[1,0,1]
	v_cvt_pk_bf16_f32 v20, v20, v21
	s_nop 0
	v_cvt_pk_bf16_f32 v21, v22, v23
	v_cvt_pk_bf16_f32 v22, v32, v33
	v_cvt_pk_bf16_f32 v23, v30, v31
	s_bitcmp1_b32 s96, 0
	s_cbranch_scc1 .Lyb_nt_3
	global_store_dwordx4 v[28:29], v[20:23], off offset:256
	s_branch .Lyb_d_3
.Lyb_nt_3:
	global_store_dwordx4 v[28:29], v[20:23], off offset:256 nt
.Lyb_d_3:
	v_pk_fma_f32 v[30:31], v[124:125], s[26:27], v[4:5] op_sel_hi:[1,0,1]
	v_pk_fma_f32 v[32:33], v[122:123], s[26:27], v[2:3] op_sel_hi:[1,0,1]
	v_or_b32_e32 v20, 32, v24
	v_ashrrev_i32_e32 v21, 31, v20
	v_lshlrev_b64 v[20:21], 12, v[20:21]
	v_lshl_add_u64 v[20:21], s[10:11], 0, v[20:21]
	v_lshl_add_u64 v[28:29], v[20:21], 0, v[26:27]
	v_pk_fma_f32 v[20:21], v[130:131], s[26:27], v[6:7] op_sel_hi:[1,0,1]
	v_pk_fma_f32 v[22:23], v[132:133], s[26:27], v[8:9] op_sel_hi:[1,0,1]
	v_cvt_pk_bf16_f32 v20, v20, v21
	s_nop 0
	v_cvt_pk_bf16_f32 v21, v22, v23
	v_cvt_pk_bf16_f32 v22, v32, v33
	v_cvt_pk_bf16_f32 v23, v30, v31
	s_bitcmp1_b32 s96, 0
	s_cbranch_scc1 .Lyb_nt_4
	global_store_dwordx4 v[28:29], v[20:23], off
	s_branch .Lyb_d_4

.Lyb_d_4:
	v_pk_fma_f32 v[30:31], v[112:113], s[26:27], v[12:13] op_sel_hi:[1,0,1]
	v_pk_fma_f32 v[32:33], v[110:111], s[26:27], v[10:11] op_sel_hi:[1,0,1]
	v_pk_fma_f32 v[20:21], v[118:119], s[26:27], v[14:15] op_sel_hi:[1,0,1]
	v_pk_fma_f32 v[22:23], v[120:121], s[26:27], v[16:17] op_sel_hi:[1,0,1]
	v_cvt_pk_bf16_f32 v20, v20, v21
	s_nop 0
	v_cvt_pk_bf16_f32 v21, v22, v23
	v_cvt_pk_bf16_f32 v22, v32, v33
	v_cvt_pk_bf16_f32 v23, v30, v31
	s_bitcmp1_b32 s96, 0
	s_cbranch_scc1 .Lyb_nt_5
	global_store_dwordx4 v[28:29], v[20:23], off offset:256
	s_branch .Lyb_d_5

.Lyb_d_5:
	v_pk_fma_f32 v[28:29], v[106:107], s[26:27], v[2:3] op_sel_hi:[1,0,1]
	s_nop 0
	v_or_b32_e32 v20, 48, v24
	v_ashrrev_i32_e32 v21, 31, v20
	v_lshlrev_b64 v[20:21], 12, v[20:21]
	v_lshl_add_u64 v[20:21], s[10:11], 0, v[20:21]
	v_lshl_add_u64 v[24:25], v[20:21], 0, v[26:27]
	v_pk_fma_f32 v[22:23], v[116:117], s[26:27], v[8:9] op_sel_hi:[1,0,1]
	v_pk_fma_f32 v[20:21], v[114:115], s[26:27], v[6:7] op_sel_hi:[1,0,1]
	v_pk_fma_f32 v[26:27], v[108:109], s[26:27], v[4:5] op_sel_hi:[1,0,1]
	v_cvt_pk_bf16_f32 v20, v20, v21
	v_cvt_pk_bf16_f32 v21, v22, v23
	v_cvt_pk_bf16_f32 v22, v28, v29
	v_pk_fma_f32 v[28:29], v[98:99], s[26:27], v[10:11] op_sel_hi:[1,0,1]
	v_cvt_pk_bf16_f32 v23, v26, v27
	s_bitcmp1_b32 s96, 0
	s_cbranch_scc1 .Lyb_nt_6
	global_store_dwordx4 v[24:25], v[20:23], off
	s_branch .Lyb_d_6
.Lyb_nt_6:
	global_store_dwordx4 v[24:25], v[20:23], off nt
.Lyb_d_6:
	v_pk_fma_f32 v[26:27], v[100:101], s[26:27], v[12:13] op_sel_hi:[1,0,1]
	s_nop 0
	v_pk_fma_f32 v[22:23], v[104:105], s[26:27], v[16:17] op_sel_hi:[1,0,1]
	v_pk_fma_f32 v[20:21], v[102:103], s[26:27], v[14:15] op_sel_hi:[1,0,1]
	s_nop 0
	v_cvt_pk_bf16_f32 v20, v20, v21
	v_cvt_pk_bf16_f32 v21, v22, v23
	v_cvt_pk_bf16_f32 v22, v28, v29
	v_cvt_pk_bf16_f32 v23, v26, v27
	s_bitcmp1_b32 s96, 0
	s_cbranch_scc1 .Lyb_nt_7
	global_store_dwordx4 v[24:25], v[20:23], off offset:256
	s_branch .Lyb_d_7
.Lyb_nt_7:
	global_store_dwordx4 v[24:25], v[20:23], off offset:256 nt
.Lyb_d_7:
	v_pk_fma_f32 v[26:27], v[92:93], s[26:27], v[4:5] op_sel_hi:[1,0,1]
	v_pk_fma_f32 v[28:29], v[90:91], s[26:27], v[2:3] op_sel_hi:[1,0,1]
	v_pk_fma_f32 v[22:23], v[96:97], s[26:27], v[8:9] op_sel_hi:[1,0,1]
	v_pk_fma_f32 v[20:21], v[94:95], s[26:27], v[6:7] op_sel_hi:[1,0,1]
	v_lshl_add_u64 v[24:25], v[18:19], 0, s[36:37]
	v_cvt_pk_bf16_f32 v20, v20, v21
	v_cvt_pk_bf16_f32 v21, v22, v23
	v_cvt_pk_bf16_f32 v22, v28, v29
	v_cvt_pk_bf16_f32 v23, v26, v27
	v_add_co_u32_e32 v26, vcc, s73, v18
	v_pk_fma_f32 v[28:29], v[78:79], s[26:27], v[10:11] op_sel_hi:[1,0,1]
	s_nop 0
	v_addc_co_u32_e32 v27, vcc, 0, v19, vcc
	s_bitcmp1_b32 s96, 0
	s_cbranch_scc1 .Lyb_nt_8
	global_store_dwordx4 v[26:27], v[20:23], off
	s_branch .Lyb_d_8
.Lyb_nt_8:
	global_store_dwordx4 v[26:27], v[20:23], off nt
.Lyb_d_8:
	v_pk_fma_f32 v[26:27], v[80:81], s[26:27], v[12:13] op_sel_hi:[1,0,1]
	s_nop 0
	v_pk_fma_f32 v[22:23], v[88:89], s[26:27], v[16:17] op_sel_hi:[1,0,1]
	v_pk_fma_f32 v[20:21], v[86:87], s[26:27], v[14:15] op_sel_hi:[1,0,1]
	s_nop 0
	v_cvt_pk_bf16_f32 v20, v20, v21
	v_cvt_pk_bf16_f32 v21, v22, v23
	v_cvt_pk_bf16_f32 v22, v28, v29
	v_cvt_pk_bf16_f32 v23, v26, v27
	s_bitcmp1_b32 s96, 0
	s_cbranch_scc1 .Lyb_nt_9
	global_store_dwordx4 v[24:25], v[20:23], off offset:256
	s_branch .Lyb_d_9

.Lyb_d_9:
	v_pk_fma_f32 v[26:27], v[76:77], s[26:27], v[4:5] op_sel_hi:[1,0,1]
	v_pk_fma_f32 v[28:29], v[74:75], s[26:27], v[2:3] op_sel_hi:[1,0,1]
	v_pk_fma_f32 v[22:23], v[84:85], s[26:27], v[8:9] op_sel_hi:[1,0,1]
	v_pk_fma_f32 v[20:21], v[82:83], s[26:27], v[6:7] op_sel_hi:[1,0,1]
	v_lshl_add_u64 v[24:25], v[18:19], 0, s[40:41]
	v_cvt_pk_bf16_f32 v20, v20, v21
	v_cvt_pk_bf16_f32 v21, v22, v23
	v_cvt_pk_bf16_f32 v22, v28, v29
	v_cvt_pk_bf16_f32 v23, v26, v27
	v_add_co_u32_e32 v26, vcc, s74, v18
	v_pk_fma_f32 v[28:29], v[62:63], s[26:27], v[10:11] op_sel_hi:[1,0,1]
	s_nop 0
	v_addc_co_u32_e32 v27, vcc, 0, v19, vcc
	s_bitcmp1_b32 s96, 0
	s_cbranch_scc1 .Lyb_nt_10
	global_store_dwordx4 v[26:27], v[20:23], off
	s_branch .Lyb_d_10

.Lyb_d_10:
	v_pk_fma_f32 v[26:27], v[64:65], s[26:27], v[12:13] op_sel_hi:[1,0,1]
	s_nop 0
	v_pk_fma_f32 v[22:23], v[72:73], s[26:27], v[16:17] op_sel_hi:[1,0,1]
	v_pk_fma_f32 v[20:21], v[70:71], s[26:27], v[14:15] op_sel_hi:[1,0,1]
	s_nop 0
	v_cvt_pk_bf16_f32 v20, v20, v21
	v_cvt_pk_bf16_f32 v21, v22, v23
	v_cvt_pk_bf16_f32 v22, v28, v29
	v_cvt_pk_bf16_f32 v23, v26, v27
	s_bitcmp1_b32 s96, 0
	s_cbranch_scc1 .Lyb_nt_11
	global_store_dwordx4 v[24:25], v[20:23], off offset:256
	s_branch .Lyb_d_11

.Lyb_d_11:
	v_pk_fma_f32 v[26:27], v[60:61], s[26:27], v[4:5] op_sel_hi:[1,0,1]
	v_pk_fma_f32 v[28:29], v[58:59], s[26:27], v[2:3] op_sel_hi:[1,0,1]
	v_pk_fma_f32 v[22:23], v[68:69], s[26:27], v[8:9] op_sel_hi:[1,0,1]
	v_pk_fma_f32 v[20:21], v[66:67], s[26:27], v[6:7] op_sel_hi:[1,0,1]
	v_lshl_add_u64 v[24:25], v[18:19], 0, s[42:43]
	v_cvt_pk_bf16_f32 v20, v20, v21
	v_cvt_pk_bf16_f32 v21, v22, v23
	v_cvt_pk_bf16_f32 v22, v28, v29
	v_cvt_pk_bf16_f32 v23, v26, v27
	v_add_co_u32_e32 v26, vcc, s75, v18
	v_pk_fma_f32 v[28:29], v[46:47], s[26:27], v[10:11] op_sel_hi:[1,0,1]
	s_nop 0
	v_addc_co_u32_e32 v27, vcc, 0, v19, vcc
	s_bitcmp1_b32 s96, 0
	s_cbranch_scc1 .Lyb_nt_12
	global_store_dwordx4 v[26:27], v[20:23], off
	s_branch .Lyb_d_12

.Lyb_d_12:
	v_pk_fma_f32 v[26:27], v[48:49], s[26:27], v[12:13] op_sel_hi:[1,0,1]
	v_pk_fma_f32 v[6:7], v[50:51], s[26:27], v[6:7] op_sel_hi:[1,0,1]
	v_pk_fma_f32 v[22:23], v[56:57], s[26:27], v[16:17] op_sel_hi:[1,0,1]
	v_pk_fma_f32 v[20:21], v[54:55], s[26:27], v[14:15] op_sel_hi:[1,0,1]
	v_pk_fma_f32 v[8:9], v[52:53], s[26:27], v[8:9] op_sel_hi:[1,0,1]
	v_cvt_pk_bf16_f32 v20, v20, v21
	v_cvt_pk_bf16_f32 v21, v22, v23
	v_cvt_pk_bf16_f32 v22, v28, v29
	v_cvt_pk_bf16_f32 v23, v26, v27
	s_bitcmp1_b32 s96, 0
	s_cbranch_scc1 .Lyb_nt_13
	global_store_dwordx4 v[24:25], v[20:23], off offset:256
	s_branch .Lyb_d_13

.Lyb_d_13:
	s_nop 1
	v_pk_fma_f32 v[22:23], v[44:45], s[26:27], v[4:5] op_sel_hi:[1,0,1]
	v_pk_fma_f32 v[4:5], v[42:43], s[26:27], v[2:3] op_sel_hi:[1,0,1]
	v_cvt_pk_bf16_f32 v2, v6, v7
	v_add_co_u32_e32 v6, vcc, s76, v18
	v_cvt_pk_bf16_f32 v3, v8, v9
	v_cvt_pk_bf16_f32 v4, v4, v5
	v_cvt_pk_bf16_f32 v5, v22, v23
	v_lshl_add_u64 v[20:21], v[18:19], 0, s[52:53]
	s_nop 0
	v_addc_co_u32_e32 v7, vcc, 0, v19, vcc
	s_bitcmp1_b32 s96, 0
	s_cbranch_scc1 .Lyb_nt_14
	global_store_dwordx4 v[6:7], v[2:5], off
	s_branch .Lyb_d_14
.Lyb_nt_14:
	global_store_dwordx4 v[6:7], v[2:5], off nt
.Lyb_d_14:
	s_andn2_b64 vcc, exec, s[54:55]
	v_pk_fma_f32 v[6:7], v[36:37], s[26:27], v[12:13] op_sel_hi:[1,0,1]
	v_pk_fma_f32 v[4:5], v[40:41], s[26:27], v[16:17] op_sel_hi:[1,0,1]
	v_pk_fma_f32 v[2:3], v[38:39], s[26:27], v[14:15] op_sel_hi:[1,0,1]
	v_pk_fma_f32 v[8:9], v[34:35], s[26:27], v[10:11] op_sel_hi:[1,0,1]
	v_cvt_pk_bf16_f32 v2, v2, v3
	v_cvt_pk_bf16_f32 v3, v4, v5
	s_nop 0
	v_cvt_pk_bf16_f32 v4, v8, v9
	v_cvt_pk_bf16_f32 v5, v6, v7
	s_bitcmp1_b32 s96, 0
	s_cbranch_scc1 .Lyb_nt_15
	global_store_dwordx4 v[20:21], v[2:5], off offset:256
	s_branch .Lyb_d_15
.Lyb_nt_15:
	global_store_dwordx4 v[20:21], v[2:5], off offset:256 nt
.Lyb_d_15:
	s_cbranch_vccnz .LBB0_2143
	s_andn2_b64 vcc, exec, s[14:15]
	s_cbranch_vccnz .LBB0_2142
	s_barrier
	s_branch .LBB0_2142
